# P5 q-up-proj epilogue: 8 rms factors preloaded at once, per-row-group load/wait chain removed (plain path), cos/sin lines warmed (rope path)
# speedup vs baseline: 1.0098x; 1.0098x over previous
;     __device__ __forceinline__ void operator()(const f32x4 (&acc)[2][2][4][2], const Unit& u, int wr, int wc, int fr, int fq) const {
;         const int row0 = u.pm * BM + wr * 64 + fr;
;         if (u.pn < 4) {
;             const int col0 = u.pn * BM + wc * 32 + 8 * fq;
; #pragma unroll
;             for (int ai = 0; ai < 2; ++ai)
; #pragma unroll
;                 for (int m = 0; m < 4; ++m) { const int row = row0 + ai * HALF + m * 16; const float sc = rq[row]; bf16_t* rowp = QM + (size_t)row * 1536 + col0;
;     ...
;                 for (int m = 0; m < 4; ++m) { const int row = row0 + ai * HALF + m * 16; const float sc = rq[row];
.LBB0_424:
	v_lshl_add_u32 v162, s36, 8, v169
	v_ashrrev_i32_e32 v163, 31, v162
	v_lshl_add_u64 v[146:147], v[162:163], 2, s[38:39]
	global_load_dword v134, v[146:147], off
	global_load_dword v210, v[146:147], off offset:64
	global_load_dword v211, v[146:147], off offset:128
	global_load_dword v212, v[146:147], off offset:192
	global_load_dword v213, v[146:147], off offset:512
	global_load_dword v214, v[146:147], off offset:576
	global_load_dword v215, v[146:147], off offset:640
	global_load_dword v216, v[146:147], off offset:704
	s_lshl_b32 s36, s37, 8
	s_cmp_gt_i32 s37, 3
	s_mov_b64 s[46:47], -1
	v_or_b32_e32 v160, 16, v162
	v_or_b32_e32 v158, 32, v162
	v_or_b32_e32 v156, 48, v162
	v_add_u32_e32 v154, 0x80, v162
	v_add_u32_e32 v152, 0x90, v162
	v_add_u32_e32 v150, 0xa0, v162
	v_add_u32_e32 v148, 0xb0, v162
	s_cbranch_scc1 .LBB0_427
	s_andn2_b64 vcc, exec, s[46:47]
	s_cbranch_vccz .LBB0_428

;     __device__ __forceinline__ void operator()(const f32x4 (&acc)[2][2][4][2], const Unit& u, int wr, int wc, int fr, int fq) const {
;     ...
;             const int head = 4 * (u.pn - 4) + wc, j0 = 8 * fq;
; #pragma unroll
;             for (int ai = 0; ai < 2; ++ai)
; #pragma unroll
;                 for (int m = 0; m < 4; ++m) { const int row = row0 + ai * HALF + m * 16; const float sc = rq[row];
;                     const f32x4 c0 = *(const f32x4*)(COS + (size_t)row * 32 + j0), c1 = *(const f32x4*)(COS + (size_t)row * 32 + j0 + 4);
;                     const f32x4 s0 = *(const f32x4*)(SIN + (size_t)row * 32 + j0), s1 = *(const f32x4*)(SIN + (size_t)row * 32 + j0 + 4);
;                     const f32x4 x1a = acc[ai][0][m][0], x1b = acc[ai][0][m][1], x2a = acc[ai][1][m][0], x2b = acc[ai][1][m][1];
;                     const f32x4 o1a = x1a * c0 - x2a * s0, o1b = x1b * c1 - x2b * s1, o2a = x2a * c0 + x1a * s0, o2b = x2b * c1 + x1b * s1;
;                     bf16_t* rowp = QM + (size_t)row * 1536 + 1024 + head * 64 + j0;
;                     *(u32x4*)(rowp) = pack8s(o1a, o1b, sc); *(u32x4*)(rowp + 32) = pack8s(o2a, o2b, sc); }
.LBB0_427:
	v_lshlrev_b64 v[164:165], 7, v[162:163]
	v_lshl_add_u64 v[184:185], v[138:139], 0, v[164:165]
	v_lshl_add_u64 v[222:223], v[138:139], 0, v[164:165]
	v_lshl_add_u64 v[224:225], v[136:137], 0, v[164:165]
	global_load_dwordx4 v[180:183], v[184:185], off
	s_nop 0
	global_load_dwordx4 v[184:187], v[184:185], off offset:16
	v_lshl_add_u64 v[164:165], v[136:137], 0, v[164:165]
	global_load_dwordx4 v[188:191], v[164:165], off
	global_load_dwordx4 v[192:195], v[164:165], off offset:16
	v_mov_b32_e32 v218, 0x1000
	v_mov_b32_e32 v219, 0
	v_mov_b32_e32 v220, 0x4000
	v_mov_b32_e32 v221, 0
	global_load_dword v226, v[222:223], off offset:2048
	global_load_dword v227, v[224:225], off offset:2048
	v_lshl_add_u64 v[228:229], v[222:223], 0, v[218:219]
	v_lshl_add_u64 v[230:231], v[224:225], 0, v[218:219]
	global_load_dword v226, v[228:229], off
	global_load_dword v227, v[230:231], off
	global_load_dword v226, v[228:229], off offset:2048
	global_load_dword v227, v[230:231], off offset:2048
	v_lshl_add_u64 v[228:229], v[222:223], 0, v[220:221]
	v_lshl_add_u64 v[230:231], v[224:225], 0, v[220:221]
	global_load_dword v226, v[228:229], off
	global_load_dword v227, v[230:231], off
	global_load_dword v226, v[228:229], off offset:2048
	global_load_dword v227, v[230:231], off offset:2048
	v_lshl_add_u64 v[228:229], v[228:229], 0, v[218:219]
	v_lshl_add_u64 v[230:231], v[230:231], 0, v[218:219]
	global_load_dword v226, v[228:229], off
	global_load_dword v227, v[230:231], off
	global_load_dword v226, v[228:229], off offset:2048
	global_load_dword v227, v[230:231], off offset:2048
	v_mov_b64_e32 v[164:165], s[24:25]
	s_add_i32 s18, s63, s36
	v_mad_i64_i32 v[196:197], s[46:47], v162, s66, v[164:165]
	s_lshl_b64 s[46:47], s[18:19], 1
	v_mov_b32_e32 v145, v135
	v_ashrrev_i32_e32 v161, 31, v160
	v_lshl_add_u64 v[196:197], v[196:197], 0, s[46:47]
	v_lshlrev_b64 v[198:199], 7, v[160:161]
	v_lshl_add_u64 v[196:197], v[196:197], 0, v[144:145]
	v_lshl_add_u64 v[200:201], v[138:139], 0, v[198:199]
	s_waitcnt vmcnt(0)
	v_pk_mul_f32 v[202:203], v[118:119], v[180:181]
	v_pk_mul_f32 v[204:205], v[120:121], v[182:183]
	v_pk_mul_f32 v[206:207], v[114:115], v[184:185]
	v_pk_mul_f32 v[208:209], v[116:117], v[186:187]
	v_pk_mul_f32 v[180:181], v[126:127], v[180:181]
	v_pk_mul_f32 v[182:183], v[128:129], v[182:183]
	v_pk_mul_f32 v[184:185], v[122:123], v[184:185]
	v_pk_mul_f32 v[186:187], v[124:125], v[186:187]
	v_pk_fma_f32 v[204:205], v[128:129], v[190:191], v[204:205] neg_lo:[0,0,1] neg_hi:[0,0,1]
	v_pk_fma_f32 v[202:203], v[126:127], v[188:189], v[202:203] neg_lo:[0,0,1] neg_hi:[0,0,1]
	v_pk_fma_f32 v[208:209], v[124:125], v[194:195], v[208:209] neg_lo:[0,0,1] neg_hi:[0,0,1]
	v_pk_fma_f32 v[206:207], v[122:123], v[192:193], v[206:207] neg_lo:[0,0,1] neg_hi:[0,0,1]
	v_pk_fma_f32 v[182:183], v[120:121], v[190:191], v[182:183]
	v_pk_fma_f32 v[180:181], v[118:119], v[188:189], v[180:181]
	v_pk_fma_f32 v[186:187], v[116:117], v[194:195], v[186:187]
	v_pk_fma_f32 v[184:185], v[114:115], v[192:193], v[184:185]
	v_mul_f32_e32 v149, v134, v202
	v_mul_f32_e32 v151, v134, v203
	v_mul_f32_e32 v153, v134, v204
	v_mul_f32_e32 v155, v134, v205
	v_mul_f32_e32 v157, v134, v206
	v_mul_f32_e32 v159, v134, v207
	v_mul_f32_e32 v163, v134, v208
	v_mul_f32_e32 v179, v134, v209
	v_mul_f32_e32 v188, v134, v180
	v_mul_f32_e32 v189, v134, v181
	v_mul_f32_e32 v190, v134, v182
	v_mul_f32_e32 v191, v134, v183
	v_cvt_pk_bf16_f32 v180, v149, v151
	v_cvt_pk_bf16_f32 v181, v153, v155
	v_cvt_pk_bf16_f32 v182, v157, v159
	v_cvt_pk_bf16_f32 v183, v163, v179
	v_mul_f32_e32 v184, v134, v184
	v_mul_f32_e32 v185, v134, v185
	v_mul_f32_e32 v186, v134, v186
	v_mul_f32_e32 v187, v134, v187
	global_store_dwordx4 v[196:197], v[180:183], off offset:2048
	v_lshl_add_u64 v[192:193], v[136:137], 0, v[198:199]
	v_ashrrev_i32_e32 v159, 31, v158
	v_cvt_pk_bf16_f32 v180, v188, v189
	v_cvt_pk_bf16_f32 v181, v190, v191
	v_cvt_pk_bf16_f32 v182, v184, v185
	v_cvt_pk_bf16_f32 v183, v186, v187
	global_store_dwordx4 v[196:197], v[180:183], off offset:2112
	global_load_dwordx4 v[180:183], v[200:201], off
	s_nop 0
	global_load_dwordx4 v[184:187], v[200:201], off offset:16
	global_load_dwordx4 v[188:191], v[192:193], off
	s_nop 0
	global_load_dwordx4 v[192:195], v[192:193], off offset:16
	v_lshl_add_u64 v[196:197], v[160:161], 2, s[38:39]
	v_mov_b32_e32 v149, v210
	v_mad_i64_i32 v[196:197], s[48:49], v160, s66, v[164:165]
	v_lshl_add_u64 v[196:197], v[196:197], 0, s[46:47]
	v_lshlrev_b64 v[198:199], 7, v[158:159]
	v_lshl_add_u64 v[196:197], v[196:197], 0, v[144:145]
	v_lshl_add_u64 v[200:201], v[138:139], 0, v[198:199]
	s_waitcnt vmcnt(0)
;     __device__ __forceinline__ void operator()(const f32x4 (&acc)[2][2][4][2], const Unit& u, int wr, int wc, int fr, int fq) const {
;     ...
;                 for (int m = 0; m < 4; ++m) { const int row = row0 + ai * HALF + m * 16; const float sc = rq[row];
;                     const f32x4 c0 = *(const f32x4*)(COS + (size_t)row * 32 + j0), c1 = *(const f32x4*)(COS + (size_t)row * 32 + j0 + 4);
;                     const f32x4 s0 = *(const f32x4*)(SIN + (size_t)row * 32 + j0), s1 = *(const f32x4*)(SIN + (size_t)row * 32 + j0 + 4);
;                     const f32x4 x1a = acc[ai][0][m][0], x1b = acc[ai][0][m][1], x2a = acc[ai][1][m][0], x2b = acc[ai][1][m][1];
;                     const f32x4 o1a = x1a * c0 - x2a * s0, o1b = x1b * c1 - x2b * s1, o2a = x2a * c0 + x1a * s0, o2b = x2b * c1 + x1b * s1;
;                     bf16_t* rowp = QM + (size_t)row * 1536 + 1024 + head * 64 + j0;
;                     *(u32x4*)(rowp) = pack8s(o1a, o1b, sc); *(u32x4*)(rowp + 32) = pack8s(o2a, o2b, sc); }
	v_pk_mul_f32 v[202:203], v[104:105], v[182:183]
	v_pk_mul_f32 v[204:205], v[102:103], v[180:181]
	v_pk_mul_f32 v[206:207], v[100:101], v[186:187]
	v_pk_mul_f32 v[208:209], v[98:99], v[184:185]
	v_pk_mul_f32 v[182:183], v[112:113], v[182:183]
	v_pk_mul_f32 v[180:181], v[110:111], v[180:181]
	v_pk_mul_f32 v[186:187], v[108:109], v[186:187]
	v_pk_mul_f32 v[184:185], v[106:107], v[184:185]
	v_pk_fma_f32 v[202:203], v[112:113], v[190:191], v[202:203] neg_lo:[0,0,1] neg_hi:[0,0,1]
	v_pk_fma_f32 v[204:205], v[110:111], v[188:189], v[204:205] neg_lo:[0,0,1] neg_hi:[0,0,1]
	v_pk_fma_f32 v[206:207], v[108:109], v[194:195], v[206:207] neg_lo:[0,0,1] neg_hi:[0,0,1]
	v_pk_fma_f32 v[208:209], v[106:107], v[192:193], v[208:209] neg_lo:[0,0,1] neg_hi:[0,0,1]
	v_pk_fma_f32 v[182:183], v[104:105], v[190:191], v[182:183]
	v_pk_fma_f32 v[180:181], v[102:103], v[188:189], v[180:181]
	v_pk_fma_f32 v[186:187], v[100:101], v[194:195], v[186:187]
	v_pk_fma_f32 v[184:185], v[98:99], v[192:193], v[184:185]
	v_mul_f32_e32 v151, v149, v204
	v_mul_f32_e32 v153, v149, v205
	v_mul_f32_e32 v155, v149, v202
	v_mul_f32_e32 v157, v149, v203
	v_mul_f32_e32 v161, v149, v208
	v_mul_f32_e32 v163, v149, v209
	v_mul_f32_e32 v179, v149, v206
	v_mul_f32_e32 v188, v149, v207
	v_mul_f32_e32 v189, v149, v180
	v_mul_f32_e32 v190, v149, v181
	v_mul_f32_e32 v191, v149, v182
	v_mul_f32_e32 v192, v149, v183
	v_cvt_pk_bf16_f32 v180, v151, v153
	v_cvt_pk_bf16_f32 v181, v155, v157
	v_cvt_pk_bf16_f32 v182, v161, v163
	v_cvt_pk_bf16_f32 v183, v179, v188
	v_mul_f32_e32 v184, v149, v184
	v_mul_f32_e32 v185, v149, v185
	v_mul_f32_e32 v186, v149, v186
	v_mul_f32_e32 v149, v149, v187
	global_store_dwordx4 v[196:197], v[180:183], off offset:2048
	v_ashrrev_i32_e32 v157, 31, v156
	s_nop 0
	v_cvt_pk_bf16_f32 v180, v189, v190
	v_cvt_pk_bf16_f32 v181, v191, v192
	v_cvt_pk_bf16_f32 v182, v184, v185
	v_cvt_pk_bf16_f32 v183, v186, v149
	global_store_dwordx4 v[196:197], v[180:183], off offset:2112
	global_load_dwordx4 v[180:183], v[200:201], off
	s_nop 0
	global_load_dwordx4 v[184:187], v[200:201], off offset:16
	v_lshl_add_u64 v[192:193], v[136:137], 0, v[198:199]
	global_load_dwordx4 v[188:191], v[192:193], off
	s_nop 0
	global_load_dwordx4 v[192:195], v[192:193], off offset:16
	v_lshl_add_u64 v[196:197], v[158:159], 2, s[38:39]
	v_mov_b32_e32 v149, v211
	v_mad_i64_i32 v[196:197], s[48:49], v158, s66, v[164:165]
	v_lshl_add_u64 v[196:197], v[196:197], 0, s[46:47]
	v_lshlrev_b64 v[198:199], 7, v[156:157]
	v_lshl_add_u64 v[196:197], v[196:197], 0, v[144:145]
	v_lshl_add_u64 v[200:201], v[138:139], 0, v[198:199]
	s_waitcnt vmcnt(0)
	v_pk_mul_f32 v[202:203], v[88:89], v[182:183]
	v_pk_mul_f32 v[204:205], v[86:87], v[180:181]
	v_pk_mul_f32 v[206:207], v[84:85], v[186:187]
	v_pk_mul_f32 v[208:209], v[82:83], v[184:185]
	v_pk_mul_f32 v[182:183], v[96:97], v[182:183]
	v_pk_mul_f32 v[180:181], v[94:95], v[180:181]
	v_pk_mul_f32 v[186:187], v[92:93], v[186:187]
	v_pk_mul_f32 v[184:185], v[90:91], v[184:185]
	v_pk_fma_f32 v[202:203], v[96:97], v[190:191], v[202:203] neg_lo:[0,0,1] neg_hi:[0,0,1]
	v_pk_fma_f32 v[204:205], v[94:95], v[188:189], v[204:205] neg_lo:[0,0,1] neg_hi:[0,0,1]
	v_pk_fma_f32 v[206:207], v[92:93], v[194:195], v[206:207] neg_lo:[0,0,1] neg_hi:[0,0,1]
	v_pk_fma_f32 v[208:209], v[90:91], v[192:193], v[208:209] neg_lo:[0,0,1] neg_hi:[0,0,1]
	v_pk_fma_f32 v[182:183], v[88:89], v[190:191], v[182:183]
	v_pk_fma_f32 v[180:181], v[86:87], v[188:189], v[180:181]
	v_pk_fma_f32 v[186:187], v[84:85], v[194:195], v[186:187]
	v_pk_fma_f32 v[184:185], v[82:83], v[192:193], v[184:185]
	v_mul_f32_e32 v151, v149, v204
	v_mul_f32_e32 v153, v149, v205
	v_mul_f32_e32 v155, v149, v202
	v_mul_f32_e32 v159, v149, v203
	v_mul_f32_e32 v161, v149, v208
	v_mul_f32_e32 v163, v149, v209
	v_mul_f32_e32 v179, v149, v206
	v_mul_f32_e32 v188, v149, v207
	v_mul_f32_e32 v189, v149, v180
	v_mul_f32_e32 v190, v149, v181
	v_mul_f32_e32 v191, v149, v182
	v_mul_f32_e32 v192, v149, v183
	v_cvt_pk_bf16_f32 v180, v151, v153
	v_cvt_pk_bf16_f32 v181, v155, v159
	v_cvt_pk_bf16_f32 v182, v161, v163
	v_cvt_pk_bf16_f32 v183, v179, v188
	v_mul_f32_e32 v184, v149, v184
	v_mul_f32_e32 v185, v149, v185
	v_mul_f32_e32 v186, v149, v186
	v_mul_f32_e32 v149, v149, v187
	global_store_dwordx4 v[196:197], v[180:183], off offset:2048
	v_ashrrev_i32_e32 v155, 31, v154
	s_nop 0
	v_cvt_pk_bf16_f32 v180, v189, v190
	v_cvt_pk_bf16_f32 v181, v191, v192
	v_cvt_pk_bf16_f32 v182, v184, v185
	v_cvt_pk_bf16_f32 v183, v186, v149
	global_store_dwordx4 v[196:197], v[180:183], off offset:2112
	global_load_dwordx4 v[180:183], v[200:201], off
	s_nop 0
	global_load_dwordx4 v[184:187], v[200:201], off offset:16
	v_lshl_add_u64 v[192:193], v[136:137], 0, v[198:199]
	global_load_dwordx4 v[188:191], v[192:193], off
	s_nop 0
	global_load_dwordx4 v[192:195], v[192:193], off offset:16
	v_lshl_add_u64 v[196:197], v[156:157], 2, s[38:39]
	v_mov_b32_e32 v149, v212
	v_mad_i64_i32 v[196:197], s[48:49], v156, s66, v[164:165]
	v_lshl_add_u64 v[196:197], v[196:197], 0, s[46:47]
	v_lshlrev_b64 v[198:199], 7, v[154:155]
	v_lshl_add_u64 v[196:197], v[196:197], 0, v[144:145]
	v_lshl_add_u64 v[200:201], v[138:139], 0, v[198:199]
	s_waitcnt vmcnt(0)
;     __device__ __forceinline__ void operator()(const f32x4 (&acc)[2][2][4][2], const Unit& u, int wr, int wc, int fr, int fq) const {
;     ...
;                 for (int m = 0; m < 4; ++m) { const int row = row0 + ai * HALF + m * 16; const float sc = rq[row];
;                     const f32x4 c0 = *(const f32x4*)(COS + (size_t)row * 32 + j0), c1 = *(const f32x4*)(COS + (size_t)row * 32 + j0 + 4);
;                     const f32x4 s0 = *(const f32x4*)(SIN + (size_t)row * 32 + j0), s1 = *(const f32x4*)(SIN + (size_t)row * 32 + j0 + 4);
;                     const f32x4 x1a = acc[ai][0][m][0], x1b = acc[ai][0][m][1], x2a = acc[ai][1][m][0], x2b = acc[ai][1][m][1];
;                     const f32x4 o1a = x1a * c0 - x2a * s0, o1b = x1b * c1 - x2b * s1, o2a = x2a * c0 + x1a * s0, o2b = x2b * c1 + x1b * s1;
;                     bf16_t* rowp = QM + (size_t)row * 1536 + 1024 + head * 64 + j0;
;                     *(u32x4*)(rowp) = pack8s(o1a, o1b, sc); *(u32x4*)(rowp + 32) = pack8s(o2a, o2b, sc); }
	v_pk_mul_f32 v[202:203], v[72:73], v[182:183]
	v_pk_mul_f32 v[204:205], v[70:71], v[180:181]
	v_pk_mul_f32 v[206:207], v[68:69], v[186:187]
	v_pk_mul_f32 v[208:209], v[66:67], v[184:185]
	v_pk_mul_f32 v[182:183], v[80:81], v[182:183]
	v_pk_mul_f32 v[180:181], v[78:79], v[180:181]
	v_pk_mul_f32 v[186:187], v[76:77], v[186:187]
	v_pk_mul_f32 v[184:185], v[74:75], v[184:185]
	v_pk_fma_f32 v[202:203], v[80:81], v[190:191], v[202:203] neg_lo:[0,0,1] neg_hi:[0,0,1]
	v_pk_fma_f32 v[204:205], v[78:79], v[188:189], v[204:205] neg_lo:[0,0,1] neg_hi:[0,0,1]
	v_pk_fma_f32 v[206:207], v[76:77], v[194:195], v[206:207] neg_lo:[0,0,1] neg_hi:[0,0,1]
	v_pk_fma_f32 v[208:209], v[74:75], v[192:193], v[208:209] neg_lo:[0,0,1] neg_hi:[0,0,1]
	v_pk_fma_f32 v[182:183], v[72:73], v[190:191], v[182:183]
	v_pk_fma_f32 v[180:181], v[70:71], v[188:189], v[180:181]
	v_pk_fma_f32 v[186:187], v[68:69], v[194:195], v[186:187]
	v_pk_fma_f32 v[184:185], v[66:67], v[192:193], v[184:185]
	v_mul_f32_e32 v151, v149, v204
	v_mul_f32_e32 v153, v149, v205
	v_mul_f32_e32 v155, v149, v202
	v_mul_f32_e32 v157, v149, v203
	v_mul_f32_e32 v159, v149, v208
	v_mul_f32_e32 v161, v149, v209
	v_mul_f32_e32 v163, v149, v206
	v_mul_f32_e32 v179, v149, v207
	v_mul_f32_e32 v188, v149, v180
	v_mul_f32_e32 v189, v149, v181
	v_mul_f32_e32 v190, v149, v182
	v_mul_f32_e32 v191, v149, v183
	v_cvt_pk_bf16_f32 v180, v151, v153
	v_cvt_pk_bf16_f32 v181, v155, v157
	v_cvt_pk_bf16_f32 v182, v159, v161
	v_cvt_pk_bf16_f32 v183, v163, v179
	v_mul_f32_e32 v184, v149, v184
	v_mul_f32_e32 v185, v149, v185
	v_mul_f32_e32 v186, v149, v186
	v_mul_f32_e32 v149, v149, v187
	global_store_dwordx4 v[196:197], v[180:183], off offset:2048
	v_lshl_add_u64 v[192:193], v[136:137], 0, v[198:199]
	v_ashrrev_i32_e32 v153, 31, v152
	v_cvt_pk_bf16_f32 v180, v188, v189
	v_cvt_pk_bf16_f32 v181, v190, v191
	v_cvt_pk_bf16_f32 v182, v184, v185
	v_cvt_pk_bf16_f32 v183, v186, v149
	global_store_dwordx4 v[196:197], v[180:183], off offset:2112
	global_load_dwordx4 v[180:183], v[200:201], off
	s_nop 0
	global_load_dwordx4 v[184:187], v[200:201], off offset:16
	global_load_dwordx4 v[188:191], v[192:193], off
	s_nop 0
	global_load_dwordx4 v[192:195], v[192:193], off offset:16
	s_nop 0
	v_mov_b32_e32 v149, v213
	v_mad_i64_i32 v[196:197], s[48:49], v154, s66, v[164:165]
	v_lshl_add_u64 v[196:197], v[196:197], 0, s[46:47]
	v_lshlrev_b64 v[198:199], 7, v[152:153]
	v_lshl_add_u64 v[196:197], v[196:197], 0, v[144:145]
	v_lshl_add_u64 v[200:201], v[138:139], 0, v[198:199]
	s_waitcnt vmcnt(0)
	v_pk_mul_f32 v[202:203], v[56:57], v[182:183]
	v_pk_mul_f32 v[204:205], v[54:55], v[180:181]
	v_pk_mul_f32 v[206:207], v[52:53], v[186:187]
	v_pk_mul_f32 v[208:209], v[50:51], v[184:185]
	v_pk_mul_f32 v[182:183], v[64:65], v[182:183]
	v_pk_mul_f32 v[180:181], v[62:63], v[180:181]
	v_pk_mul_f32 v[186:187], v[60:61], v[186:187]
	v_pk_mul_f32 v[184:185], v[58:59], v[184:185]
	v_pk_fma_f32 v[202:203], v[64:65], v[190:191], v[202:203] neg_lo:[0,0,1] neg_hi:[0,0,1]
	v_pk_fma_f32 v[204:205], v[62:63], v[188:189], v[204:205] neg_lo:[0,0,1] neg_hi:[0,0,1]
	v_pk_fma_f32 v[206:207], v[60:61], v[194:195], v[206:207] neg_lo:[0,0,1] neg_hi:[0,0,1]
	v_pk_fma_f32 v[208:209], v[58:59], v[192:193], v[208:209] neg_lo:[0,0,1] neg_hi:[0,0,1]
	v_pk_fma_f32 v[182:183], v[56:57], v[190:191], v[182:183]
	v_pk_fma_f32 v[180:181], v[54:55], v[188:189], v[180:181]
	v_pk_fma_f32 v[186:187], v[52:53], v[194:195], v[186:187]
	v_pk_fma_f32 v[184:185], v[50:51], v[192:193], v[184:185]
	v_mul_f32_e32 v151, v149, v204
	v_mul_f32_e32 v153, v149, v205
	v_mul_f32_e32 v155, v149, v202
	v_mul_f32_e32 v157, v149, v203
	v_mul_f32_e32 v159, v149, v208
	v_mul_f32_e32 v161, v149, v209
	v_mul_f32_e32 v163, v149, v206
	v_mul_f32_e32 v179, v149, v207
	v_mul_f32_e32 v188, v149, v180
	v_mul_f32_e32 v189, v149, v181
	v_mul_f32_e32 v190, v149, v182
	v_mul_f32_e32 v191, v149, v183
	v_cvt_pk_bf16_f32 v180, v151, v153
	v_cvt_pk_bf16_f32 v181, v155, v157
	v_cvt_pk_bf16_f32 v182, v159, v161
	v_cvt_pk_bf16_f32 v183, v163, v179
	v_mul_f32_e32 v184, v149, v184
	v_mul_f32_e32 v185, v149, v185
	v_mul_f32_e32 v186, v149, v186
	v_mul_f32_e32 v149, v149, v187
	global_store_dwordx4 v[196:197], v[180:183], off offset:2048
	v_lshl_add_u64 v[192:193], v[136:137], 0, v[198:199]
	v_ashrrev_i32_e32 v151, 31, v150
	v_cvt_pk_bf16_f32 v180, v188, v189
	v_cvt_pk_bf16_f32 v181, v190, v191
	v_cvt_pk_bf16_f32 v182, v184, v185
	v_cvt_pk_bf16_f32 v183, v186, v149
	global_store_dwordx4 v[196:197], v[180:183], off offset:2112
	global_load_dwordx4 v[180:183], v[200:201], off
	s_nop 0
	global_load_dwordx4 v[184:187], v[200:201], off offset:16
	global_load_dwordx4 v[188:191], v[192:193], off
	s_nop 0
	global_load_dwordx4 v[192:195], v[192:193], off offset:16
	s_nop 0
	v_mov_b32_e32 v149, v214
	v_mad_i64_i32 v[196:197], s[48:49], v152, s66, v[164:165]
	v_lshl_add_u64 v[196:197], v[196:197], 0, s[46:47]
	v_lshlrev_b64 v[198:199], 7, v[150:151]
	v_lshl_add_u64 v[196:197], v[196:197], 0, v[144:145]
	v_lshl_add_u64 v[200:201], v[138:139], 0, v[198:199]
	s_waitcnt vmcnt(0)
;     __device__ __forceinline__ void operator()(const f32x4 (&acc)[2][2][4][2], const Unit& u, int wr, int wc, int fr, int fq) const {
;     ...
;             const int head = 4 * (u.pn - 4) + wc, j0 = 8 * fq;
; #pragma unroll
;             for (int ai = 0; ai < 2; ++ai)
; #pragma unroll
;                 for (int m = 0; m < 4; ++m) { const int row = row0 + ai * HALF + m * 16; const float sc = rq[row];
;                     const f32x4 c0 = *(const f32x4*)(COS + (size_t)row * 32 + j0), c1 = *(const f32x4*)(COS + (size_t)row * 32 + j0 + 4);
;                     const f32x4 s0 = *(const f32x4*)(SIN + (size_t)row * 32 + j0), s1 = *(const f32x4*)(SIN + (size_t)row * 32 + j0 + 4);
;                     const f32x4 x1a = acc[ai][0][m][0], x1b = acc[ai][0][m][1], x2a = acc[ai][1][m][0], x2b = acc[ai][1][m][1];
;                     const f32x4 o1a = x1a * c0 - x2a * s0, o1b = x1b * c1 - x2b * s1, o2a = x2a * c0 + x1a * s0, o2b = x2b * c1 + x1b * s1;
;                     bf16_t* rowp = QM + (size_t)row * 1536 + 1024 + head * 64 + j0;
;                     *(u32x4*)(rowp) = pack8s(o1a, o1b, sc); *(u32x4*)(rowp + 32) = pack8s(o2a, o2b, sc); }
	v_pk_mul_f32 v[202:203], v[40:41], v[182:183]
	v_pk_mul_f32 v[204:205], v[38:39], v[180:181]
	v_pk_mul_f32 v[206:207], v[36:37], v[186:187]
	v_pk_mul_f32 v[208:209], v[34:35], v[184:185]
	v_pk_mul_f32 v[182:183], v[48:49], v[182:183]
	v_pk_mul_f32 v[180:181], v[46:47], v[180:181]
	v_pk_mul_f32 v[186:187], v[44:45], v[186:187]
	v_pk_mul_f32 v[184:185], v[42:43], v[184:185]
	v_pk_fma_f32 v[202:203], v[48:49], v[190:191], v[202:203] neg_lo:[0,0,1] neg_hi:[0,0,1]
	v_pk_fma_f32 v[204:205], v[46:47], v[188:189], v[204:205] neg_lo:[0,0,1] neg_hi:[0,0,1]
	v_pk_fma_f32 v[206:207], v[44:45], v[194:195], v[206:207] neg_lo:[0,0,1] neg_hi:[0,0,1]
	v_pk_fma_f32 v[208:209], v[42:43], v[192:193], v[208:209] neg_lo:[0,0,1] neg_hi:[0,0,1]
	v_pk_fma_f32 v[182:183], v[40:41], v[190:191], v[182:183]
	v_pk_fma_f32 v[180:181], v[38:39], v[188:189], v[180:181]
	v_pk_fma_f32 v[186:187], v[36:37], v[194:195], v[186:187]
	v_pk_fma_f32 v[184:185], v[34:35], v[192:193], v[184:185]
	v_mul_f32_e32 v151, v149, v204
	v_mul_f32_e32 v153, v149, v205
	v_mul_f32_e32 v155, v149, v202
	v_mul_f32_e32 v157, v149, v203
	v_mul_f32_e32 v159, v149, v208
	v_mul_f32_e32 v161, v149, v209
	v_mul_f32_e32 v163, v149, v206
	v_mul_f32_e32 v179, v149, v207
	v_mul_f32_e32 v188, v149, v180
	v_mul_f32_e32 v189, v149, v181
	v_mul_f32_e32 v190, v149, v182
	v_mul_f32_e32 v191, v149, v183
	v_cvt_pk_bf16_f32 v180, v151, v153
	v_cvt_pk_bf16_f32 v181, v155, v157
	v_cvt_pk_bf16_f32 v182, v159, v161
	v_cvt_pk_bf16_f32 v183, v163, v179
	v_mul_f32_e32 v184, v149, v184
	v_mul_f32_e32 v185, v149, v185
	v_mul_f32_e32 v186, v149, v186
	v_mul_f32_e32 v149, v149, v187
	global_store_dwordx4 v[196:197], v[180:183], off offset:2048
	v_lshl_add_u64 v[192:193], v[136:137], 0, v[198:199]
	s_nop 0
	v_cvt_pk_bf16_f32 v180, v188, v189
	v_cvt_pk_bf16_f32 v181, v190, v191
	v_cvt_pk_bf16_f32 v182, v184, v185
	v_cvt_pk_bf16_f32 v183, v186, v149
	global_store_dwordx4 v[196:197], v[180:183], off offset:2112
	global_load_dwordx4 v[180:183], v[200:201], off
	s_nop 0
	global_load_dwordx4 v[184:187], v[200:201], off offset:16
	global_load_dwordx4 v[188:191], v[192:193], off
	s_nop 0
	global_load_dwordx4 v[192:195], v[192:193], off offset:16
	s_nop 0
	v_mov_b32_e32 v151, v215
	v_mad_i64_i32 v[196:197], s[48:49], v150, s66, v[164:165]
	v_ashrrev_i32_e32 v149, 31, v148
	v_lshl_add_u64 v[196:197], v[196:197], 0, s[46:47]
	v_lshlrev_b64 v[198:199], 7, v[148:149]
	v_lshl_add_u64 v[196:197], v[196:197], 0, v[144:145]
	v_lshl_add_u64 v[200:201], v[138:139], 0, v[198:199]
	v_mad_i64_i32 v[164:165], s[48:49], v148, s66, v[164:165]
	v_lshl_add_u64 v[164:165], v[164:165], 0, s[46:47]
	v_lshl_add_u64 v[164:165], v[164:165], 0, v[144:145]
	s_waitcnt vmcnt(0)
	v_pk_mul_f32 v[202:203], v[24:25], v[182:183]
	v_pk_mul_f32 v[204:205], v[22:23], v[180:181]
	v_pk_mul_f32 v[206:207], v[20:21], v[186:187]
	v_pk_mul_f32 v[208:209], v[18:19], v[184:185]
	v_pk_mul_f32 v[182:183], v[32:33], v[182:183]
	v_pk_mul_f32 v[180:181], v[30:31], v[180:181]
	v_pk_mul_f32 v[186:187], v[28:29], v[186:187]
	v_pk_mul_f32 v[184:185], v[26:27], v[184:185]
	v_pk_fma_f32 v[202:203], v[32:33], v[190:191], v[202:203] neg_lo:[0,0,1] neg_hi:[0,0,1]
	v_pk_fma_f32 v[204:205], v[30:31], v[188:189], v[204:205] neg_lo:[0,0,1] neg_hi:[0,0,1]
	v_pk_fma_f32 v[206:207], v[28:29], v[194:195], v[206:207] neg_lo:[0,0,1] neg_hi:[0,0,1]
	v_pk_fma_f32 v[208:209], v[26:27], v[192:193], v[208:209] neg_lo:[0,0,1] neg_hi:[0,0,1]
	v_pk_fma_f32 v[182:183], v[24:25], v[190:191], v[182:183]
	v_pk_fma_f32 v[180:181], v[22:23], v[188:189], v[180:181]
	v_pk_fma_f32 v[186:187], v[20:21], v[194:195], v[186:187]
	v_pk_fma_f32 v[184:185], v[18:19], v[192:193], v[184:185]
	v_mul_f32_e32 v149, v151, v204
	v_mul_f32_e32 v153, v151, v205
	v_mul_f32_e32 v155, v151, v202
	v_mul_f32_e32 v157, v151, v203
	v_mul_f32_e32 v159, v151, v208
	v_mul_f32_e32 v161, v151, v209
	v_mul_f32_e32 v163, v151, v206
	v_mul_f32_e32 v179, v151, v207
	v_mul_f32_e32 v188, v151, v180
	v_mul_f32_e32 v189, v151, v181
	v_mul_f32_e32 v190, v151, v182
	v_mul_f32_e32 v191, v151, v183
	v_cvt_pk_bf16_f32 v180, v149, v153
	v_cvt_pk_bf16_f32 v181, v155, v157
	v_cvt_pk_bf16_f32 v182, v159, v161
	v_cvt_pk_bf16_f32 v183, v163, v179
	v_mul_f32_e32 v184, v151, v184
	v_mul_f32_e32 v185, v151, v185
	v_mul_f32_e32 v186, v151, v186
	v_mul_f32_e32 v151, v151, v187
	global_store_dwordx4 v[196:197], v[180:183], off offset:2048
	v_lshl_add_u64 v[192:193], v[136:137], 0, v[198:199]
	s_nop 0
	v_cvt_pk_bf16_f32 v180, v188, v189
	v_cvt_pk_bf16_f32 v181, v190, v191
	v_cvt_pk_bf16_f32 v182, v184, v185
	v_cvt_pk_bf16_f32 v183, v186, v151
	global_store_dwordx4 v[196:197], v[180:183], off offset:2112
	global_load_dwordx4 v[180:183], v[200:201], off
	s_nop 0
	global_load_dwordx4 v[184:187], v[200:201], off offset:16
	global_load_dwordx4 v[188:191], v[192:193], off
	s_nop 0
	global_load_dwordx4 v[192:195], v[192:193], off offset:16
	s_nop 0
	v_mov_b32_e32 v149, v216
	s_waitcnt vmcnt(0)
	v_pk_mul_f32 v[196:197], v[8:9], v[182:183]
	v_pk_mul_f32 v[198:199], v[6:7], v[180:181]
	v_pk_mul_f32 v[200:201], v[4:5], v[186:187]
	v_pk_mul_f32 v[202:203], v[2:3], v[184:185]
	v_pk_mul_f32 v[182:183], v[16:17], v[182:183]
	v_pk_mul_f32 v[180:181], v[14:15], v[180:181]
	v_pk_mul_f32 v[186:187], v[12:13], v[186:187]
	v_pk_mul_f32 v[184:185], v[10:11], v[184:185]
	v_pk_fma_f32 v[196:197], v[16:17], v[190:191], v[196:197] neg_lo:[0,0,1] neg_hi:[0,0,1]
	v_pk_fma_f32 v[198:199], v[14:15], v[188:189], v[198:199] neg_lo:[0,0,1] neg_hi:[0,0,1]
	v_pk_fma_f32 v[200:201], v[12:13], v[194:195], v[200:201] neg_lo:[0,0,1] neg_hi:[0,0,1]
	v_pk_fma_f32 v[202:203], v[10:11], v[192:193], v[202:203] neg_lo:[0,0,1] neg_hi:[0,0,1]
	v_pk_fma_f32 v[182:183], v[8:9], v[190:191], v[182:183]
	v_pk_fma_f32 v[180:181], v[6:7], v[188:189], v[180:181]
	v_pk_fma_f32 v[186:187], v[4:5], v[194:195], v[186:187]
	v_pk_fma_f32 v[184:185], v[2:3], v[192:193], v[184:185]
	v_mul_f32_e32 v145, v149, v198
	v_mul_f32_e32 v151, v149, v199
	v_mul_f32_e32 v153, v149, v196
	v_mul_f32_e32 v155, v149, v197
	v_mul_f32_e32 v157, v149, v202
	v_mul_f32_e32 v159, v149, v203
	v_mul_f32_e32 v161, v149, v200
	v_mul_f32_e32 v163, v149, v201
	v_mul_f32_e32 v179, v149, v180
	v_mul_f32_e32 v188, v149, v181
	v_mul_f32_e32 v189, v149, v182
	v_mul_f32_e32 v190, v149, v183
	v_cvt_pk_bf16_f32 v180, v145, v151
	v_cvt_pk_bf16_f32 v181, v153, v155
	v_cvt_pk_bf16_f32 v182, v157, v159
	v_cvt_pk_bf16_f32 v183, v161, v163
	v_mul_f32_e32 v184, v149, v184
	v_mul_f32_e32 v185, v149, v185
	v_mul_f32_e32 v186, v149, v186
	v_mul_f32_e32 v149, v149, v187
	global_store_dwordx4 v[164:165], v[180:183], off offset:2048
	s_nop 1
	v_cvt_pk_bf16_f32 v180, v179, v188
	v_cvt_pk_bf16_f32 v181, v189, v190
	v_cvt_pk_bf16_f32 v182, v184, v185
	v_cvt_pk_bf16_f32 v183, v186, v149
	global_store_dwordx4 v[164:165], v[180:183], off offset:2112
	s_cbranch_execnz .LBB0_426
;     __device__ __forceinline__ void operator()(const f32x4 (&acc)[2][2][4][2], const Unit& u, int wr, int wc, int fr, int fq) const {
;     ...
;         if (u.pn < 4) {
;             const int col0 = u.pn * BM + wc * 32 + 8 * fq;
; #pragma unroll
;             for (int ai = 0; ai < 2; ++ai)
; #pragma unroll
;                 for (int m = 0; m < 4; ++m) { const int row = row0 + ai * HALF + m * 16; const float sc = rq[row]; bf16_t* rowp = QM + (size_t)row * 1536 + col0;
; #pragma unroll
;                     for (int bj = 0; bj < 2; ++bj) *(u32x4*)(rowp + bj * HALF) = pack8s(acc[ai][bj][m][0], acc[ai][bj][m][1], sc); }
.LBB0_428:
	s_nop 0
	v_or_b32_e32 v180, s36, v171
	v_ashrrev_i32_e32 v181, 31, v180
	v_mov_b64_e32 v[164:165], s[24:25]
	v_mad_i64_i32 v[182:183], s[36:37], v162, s66, v[164:165]
	v_lshlrev_b64 v[162:163], 1, v[180:181]
	s_waitcnt vmcnt(0)
	v_mul_f32_e32 v126, v126, v134
	v_mul_f32_e32 v127, v127, v134
	v_lshl_add_u64 v[180:181], v[182:183], 0, v[162:163]
	v_cvt_pk_bf16_f32 v126, v126, v127
	v_mul_f32_e32 v127, v128, v134
	v_mul_f32_e32 v128, v129, v134
	v_mul_f32_e32 v122, v122, v134
	v_mul_f32_e32 v123, v123, v134
	v_mul_f32_e32 v118, v118, v134
	v_mul_f32_e32 v119, v119, v134
	v_cvt_pk_bf16_f32 v127, v127, v128
	v_cvt_pk_bf16_f32 v128, v122, v123
	v_mul_f32_e32 v122, v124, v134
	v_mul_f32_e32 v123, v125, v134
	v_cvt_pk_bf16_f32 v129, v122, v123
	global_store_dwordx4 v[180:181], v[126:129], off
	v_cvt_pk_bf16_f32 v118, v118, v119
	v_mul_f32_e32 v119, v120, v134
	v_mul_f32_e32 v120, v121, v134
	v_mul_f32_e32 v114, v114, v134
	v_mul_f32_e32 v115, v115, v134
	v_cvt_pk_bf16_f32 v119, v119, v120
	v_cvt_pk_bf16_f32 v120, v114, v115
	v_mul_f32_e32 v114, v116, v134
	v_mul_f32_e32 v115, v117, v134
	v_ashrrev_i32_e32 v161, 31, v160
	v_cvt_pk_bf16_f32 v121, v114, v115
	global_store_dwordx4 v[180:181], v[118:121], off offset:256
	v_lshl_add_u64 v[114:115], v[160:161], 2, s[38:39]
	s_nop 1
	v_mov_b32_e32 v118, v210
	v_mad_i64_i32 v[114:115], s[36:37], v160, s66, v[164:165]
	v_ashrrev_i32_e32 v159, 31, v158
	v_lshl_add_u64 v[114:115], v[114:115], 0, v[162:163]
	v_lshl_add_u64 v[116:117], v[158:159], 2, s[38:39]
	v_ashrrev_i32_e32 v157, 31, v156
	s_nop 1
	v_mul_f32_e32 v110, v110, v118
	v_mul_f32_e32 v111, v111, v118
	v_mul_f32_e32 v112, v112, v118
	v_mul_f32_e32 v113, v113, v118
	v_mul_f32_e32 v106, v106, v118
	v_mul_f32_e32 v107, v107, v118
	v_mul_f32_e32 v108, v108, v118
	v_mul_f32_e32 v109, v109, v118
	v_mul_f32_e32 v102, v102, v118
	v_mul_f32_e32 v103, v103, v118
	v_mul_f32_e32 v104, v104, v118
	v_mul_f32_e32 v105, v105, v118
	v_mul_f32_e32 v119, v98, v118
	v_mul_f32_e32 v120, v99, v118
	v_mul_f32_e32 v121, v100, v118
	v_mul_f32_e32 v118, v101, v118
	v_cvt_pk_bf16_f32 v98, v110, v111
	v_cvt_pk_bf16_f32 v99, v112, v113
	v_cvt_pk_bf16_f32 v100, v106, v107
	v_cvt_pk_bf16_f32 v101, v108, v109
	global_store_dwordx4 v[114:115], v[98:101], off
	s_nop 1
	v_cvt_pk_bf16_f32 v98, v102, v103
	v_cvt_pk_bf16_f32 v99, v104, v105
	v_cvt_pk_bf16_f32 v100, v119, v120
	v_cvt_pk_bf16_f32 v101, v121, v118
	global_store_dwordx4 v[114:115], v[98:101], off offset:256
	s_nop 1
	v_mov_b32_e32 v102, v211
	s_nop 1
	v_mul_f32_e32 v94, v94, v102
	v_mad_i64_i32 v[98:99], s[36:37], v158, s66, v[164:165]
	v_lshl_add_u64 v[98:99], v[98:99], 0, v[162:163]
	v_mul_f32_e32 v95, v95, v102
	v_mul_f32_e32 v96, v96, v102
	v_mul_f32_e32 v97, v97, v102
	v_mul_f32_e32 v90, v90, v102
	v_mul_f32_e32 v91, v91, v102
	v_mul_f32_e32 v92, v92, v102
	v_mul_f32_e32 v93, v93, v102
	v_mul_f32_e32 v86, v86, v102
	v_mul_f32_e32 v87, v87, v102
	v_mul_f32_e32 v88, v88, v102
	v_mul_f32_e32 v89, v89, v102
	v_mul_f32_e32 v103, v82, v102
	v_mul_f32_e32 v104, v83, v102
	v_mul_f32_e32 v105, v84, v102
	v_mul_f32_e32 v102, v85, v102
	v_cvt_pk_bf16_f32 v82, v94, v95
	v_cvt_pk_bf16_f32 v83, v96, v97
	v_cvt_pk_bf16_f32 v84, v90, v91
	v_cvt_pk_bf16_f32 v85, v92, v93
	v_lshl_add_u64 v[100:101], v[156:157], 2, s[38:39]
	global_store_dwordx4 v[98:99], v[82:85], off
	s_nop 1
	v_cvt_pk_bf16_f32 v82, v86, v87
	v_cvt_pk_bf16_f32 v83, v88, v89
	v_cvt_pk_bf16_f32 v84, v103, v104
	v_cvt_pk_bf16_f32 v85, v105, v102
	global_store_dwordx4 v[98:99], v[82:85], off offset:256
	s_nop 1
	v_mov_b32_e32 v84, v212
	s_nop 1
	v_mul_f32_e32 v78, v78, v84
	v_mad_i64_i32 v[82:83], s[36:37], v156, s66, v[164:165]
	v_lshl_add_u64 v[82:83], v[82:83], 0, v[162:163]
	v_mul_f32_e32 v79, v79, v84
	v_mul_f32_e32 v80, v80, v84
	v_mul_f32_e32 v81, v81, v84
	v_mul_f32_e32 v74, v74, v84
	v_mul_f32_e32 v75, v75, v84
	v_mul_f32_e32 v76, v76, v84
	v_mul_f32_e32 v77, v77, v84
	v_mul_f32_e32 v70, v70, v84
	v_mul_f32_e32 v71, v71, v84
	v_mul_f32_e32 v72, v72, v84
	v_mul_f32_e32 v73, v73, v84
	v_mul_f32_e32 v85, v66, v84
	v_mul_f32_e32 v86, v67, v84
	v_mul_f32_e32 v87, v68, v84
	v_mul_f32_e32 v84, v69, v84
	v_cvt_pk_bf16_f32 v66, v78, v79
	v_cvt_pk_bf16_f32 v67, v80, v81
	v_cvt_pk_bf16_f32 v68, v74, v75
;     __device__ __forceinline__ void operator()(const f32x4 (&acc)[2][2][4][2], const Unit& u, int wr, int wc, int fr, int fq) const {
;     ...
;             for (int ai = 0; ai < 2; ++ai)
; #pragma unroll
;                 for (int m = 0; m < 4; ++m) { const int row = row0 + ai * HALF + m * 16; const float sc = rq[row]; bf16_t* rowp = QM + (size_t)row * 1536 + col0;
; #pragma unroll
;                     for (int bj = 0; bj < 2; ++bj) *(u32x4*)(rowp + bj * HALF) = pack8s(acc[ai][bj][m][0], acc[ai][bj][m][1], sc); }
	v_cvt_pk_bf16_f32 v69, v76, v77
	global_store_dwordx4 v[82:83], v[66:69], off
	s_nop 1
	v_cvt_pk_bf16_f32 v66, v70, v71
	v_cvt_pk_bf16_f32 v67, v72, v73
	v_cvt_pk_bf16_f32 v68, v85, v86
	v_cvt_pk_bf16_f32 v69, v87, v84
	global_store_dwordx4 v[82:83], v[66:69], off offset:256
	s_nop 1
	v_mov_b32_e32 v68, v213
	s_nop 1
	v_mul_f32_e32 v62, v62, v68
	v_mad_i64_i32 v[66:67], s[36:37], v154, s66, v[164:165]
	v_lshl_add_u64 v[66:67], v[66:67], 0, v[162:163]
	v_mul_f32_e32 v63, v63, v68
	v_mul_f32_e32 v64, v64, v68
	v_mul_f32_e32 v65, v65, v68
	v_mul_f32_e32 v58, v58, v68
	v_mul_f32_e32 v59, v59, v68
	v_mul_f32_e32 v60, v60, v68
	v_mul_f32_e32 v61, v61, v68
	v_mul_f32_e32 v54, v54, v68
	v_mul_f32_e32 v55, v55, v68
	v_mul_f32_e32 v56, v56, v68
	v_mul_f32_e32 v57, v57, v68
	v_mul_f32_e32 v69, v50, v68
	v_mul_f32_e32 v70, v51, v68
	v_mul_f32_e32 v71, v52, v68
	v_mul_f32_e32 v68, v53, v68
	v_cvt_pk_bf16_f32 v50, v62, v63
	v_cvt_pk_bf16_f32 v51, v64, v65
	v_cvt_pk_bf16_f32 v52, v58, v59
	v_cvt_pk_bf16_f32 v53, v60, v61
	global_store_dwordx4 v[66:67], v[50:53], off
	s_nop 1
	v_cvt_pk_bf16_f32 v50, v54, v55
	v_cvt_pk_bf16_f32 v51, v56, v57
	v_cvt_pk_bf16_f32 v52, v69, v70
	v_cvt_pk_bf16_f32 v53, v71, v68
	global_store_dwordx4 v[66:67], v[50:53], off offset:256
	s_nop 1
	v_mov_b32_e32 v52, v214
	s_nop 1
	v_mul_f32_e32 v46, v46, v52
	v_mad_i64_i32 v[50:51], s[36:37], v152, s66, v[164:165]
	v_lshl_add_u64 v[50:51], v[50:51], 0, v[162:163]
	v_mul_f32_e32 v47, v47, v52
	v_mul_f32_e32 v48, v48, v52
	v_mul_f32_e32 v49, v49, v52
	v_mul_f32_e32 v42, v42, v52
	v_mul_f32_e32 v43, v43, v52
	v_mul_f32_e32 v44, v44, v52
	v_mul_f32_e32 v45, v45, v52
	v_mul_f32_e32 v38, v38, v52
	v_mul_f32_e32 v39, v39, v52
	v_mul_f32_e32 v40, v40, v52
	v_mul_f32_e32 v41, v41, v52
	v_mul_f32_e32 v53, v34, v52
	v_mul_f32_e32 v54, v35, v52
	v_mul_f32_e32 v55, v36, v52
	v_mul_f32_e32 v52, v37, v52
	v_cvt_pk_bf16_f32 v34, v46, v47
	v_cvt_pk_bf16_f32 v35, v48, v49
	v_cvt_pk_bf16_f32 v36, v42, v43
	v_cvt_pk_bf16_f32 v37, v44, v45
	global_store_dwordx4 v[50:51], v[34:37], off
	s_nop 1
	v_cvt_pk_bf16_f32 v34, v38, v39
	v_cvt_pk_bf16_f32 v35, v40, v41
	v_cvt_pk_bf16_f32 v36, v53, v54
	v_cvt_pk_bf16_f32 v37, v55, v52
	global_store_dwordx4 v[50:51], v[34:37], off offset:256
	s_nop 1
	v_mov_b32_e32 v36, v215
	s_nop 1
	v_mul_f32_e32 v30, v30, v36
	v_mad_i64_i32 v[34:35], s[36:37], v150, s66, v[164:165]
	v_lshl_add_u64 v[34:35], v[34:35], 0, v[162:163]
	v_mul_f32_e32 v31, v31, v36
	v_mul_f32_e32 v32, v32, v36
	v_mul_f32_e32 v33, v33, v36
	v_mul_f32_e32 v26, v26, v36
	v_mul_f32_e32 v27, v27, v36
	v_mul_f32_e32 v28, v28, v36
	v_mul_f32_e32 v29, v29, v36
	v_mul_f32_e32 v22, v22, v36
	v_mul_f32_e32 v23, v23, v36
	v_mul_f32_e32 v24, v24, v36
	v_mul_f32_e32 v25, v25, v36
	v_mul_f32_e32 v37, v18, v36
	v_mul_f32_e32 v38, v19, v36
	v_mul_f32_e32 v39, v20, v36
	v_mul_f32_e32 v36, v21, v36
	v_cvt_pk_bf16_f32 v18, v30, v31
	v_cvt_pk_bf16_f32 v19, v32, v33
	v_cvt_pk_bf16_f32 v20, v26, v27
	v_cvt_pk_bf16_f32 v21, v28, v29
	global_store_dwordx4 v[34:35], v[18:21], off
	s_nop 1
	v_cvt_pk_bf16_f32 v18, v22, v23
	v_cvt_pk_bf16_f32 v19, v24, v25
	v_cvt_pk_bf16_f32 v20, v37, v38
	v_cvt_pk_bf16_f32 v21, v39, v36
	global_store_dwordx4 v[34:35], v[18:21], off offset:256
	s_nop 1
	v_mov_b32_e32 v20, v216
	s_nop 1
	v_mul_f32_e32 v14, v14, v20
	v_mad_i64_i32 v[18:19], s[36:37], v148, s66, v[164:165]
	v_lshl_add_u64 v[18:19], v[18:19], 0, v[162:163]
	v_mul_f32_e32 v15, v15, v20
	v_mul_f32_e32 v16, v16, v20
	v_mul_f32_e32 v17, v17, v20
	v_mul_f32_e32 v10, v10, v20
	v_mul_f32_e32 v11, v11, v20
	v_mul_f32_e32 v12, v12, v20
	v_mul_f32_e32 v13, v13, v20
	v_mul_f32_e32 v6, v6, v20
	v_mul_f32_e32 v7, v7, v20
	v_mul_f32_e32 v8, v8, v20
	v_mul_f32_e32 v9, v9, v20
	v_mul_f32_e32 v21, v2, v20
	v_mul_f32_e32 v22, v3, v20
	v_mul_f32_e32 v23, v4, v20
	v_mul_f32_e32 v20, v5, v20
	v_cvt_pk_bf16_f32 v2, v14, v15
	v_cvt_pk_bf16_f32 v3, v16, v17
	v_cvt_pk_bf16_f32 v4, v10, v11
	v_cvt_pk_bf16_f32 v5, v12, v13
	global_store_dwordx4 v[18:19], v[2:5], off
	s_nop 1
	v_cvt_pk_bf16_f32 v2, v6, v7
	v_cvt_pk_bf16_f32 v3, v8, v9
	v_cvt_pk_bf16_f32 v4, v21, v22
	v_cvt_pk_bf16_f32 v5, v23, v20
	global_store_dwordx4 v[18:19], v[2:5], off offset:256
	s_and_b64 vcc, exec, s[4:5]
	s_mov_b64 s[4:5], -1
	s_cbranch_vccnz .LBB0_412
